# union: dense loop v3b, banded wait fix, barriers polling the arrival counter, LSE-combine loop with the next token's loads in flight
# speedup vs baseline: 1.0132x; 1.0093x over previous
.LBB0_599:
	s_waitcnt lgkmcnt(0)
	v_lshl_add_u64 v[28:29], s[0:1], 0, v[12:13]
	v_lshl_add_u64 v[30:31], s[0:1], 0, v[8:9]
	v_lshl_add_u64 v[32:33], s[0:1], 0, v[4:5]
	v_lshl_add_u64 v[34:35], s[0:1], 0, v[10:11]
	v_lshl_add_u64 v[36:37], s[0:1], 0, v[6:7]
	v_lshl_add_u64 v[38:39], s[0:1], 0, v[2:3]
	global_load_dword v44, v[28:29], off
	global_load_dword v45, v[30:31], off
	global_load_dword v46, v[32:33], off
	global_load_dwordx4 v[16:19], v[34:35], off
	global_load_dwordx4 v[20:23], v[36:37], off
	global_load_dwordx4 v[24:27], v[38:39], off
	s_add_i32 s12, s12, s56
	v_lshl_add_u64 v[42:43], s[0:1], 0, v[14:15]
	v_lshl_add_u64 v[2:3], v[2:3], 0, s[4:5]
	v_lshl_add_u64 v[4:5], v[4:5], 0, s[6:7]
	v_lshl_add_u64 v[6:7], v[6:7], 0, s[4:5]
	v_lshl_add_u64 v[8:9], v[8:9], 0, s[6:7]
	v_lshl_add_u64 v[10:11], v[10:11], 0, s[4:5]
	v_lshl_add_u64 v[12:13], v[12:13], 0, s[6:7]
	v_lshl_add_u64 v[14:15], v[14:15], 0, s[8:9]
	v_lshl_add_u64 v[28:29], s[0:1], 0, v[12:13]
	v_lshl_add_u64 v[30:31], s[0:1], 0, v[8:9]
	v_lshl_add_u64 v[32:33], s[0:1], 0, v[4:5]
	v_lshl_add_u64 v[34:35], s[0:1], 0, v[10:11]
	v_lshl_add_u64 v[36:37], s[0:1], 0, v[6:7]
	v_lshl_add_u64 v[38:39], s[0:1], 0, v[2:3]
	global_load_dword v60, v[28:29], off
	global_load_dword v61, v[30:31], off
	global_load_dword v62, v[32:33], off
	global_load_dwordx4 v[64:67], v[34:35], off
	global_load_dwordx4 v[68:71], v[36:37], off
	global_load_dwordx4 v[72:75], v[38:39], off
	s_add_i32 s12, s12, s56
	v_lshl_add_u64 v[58:59], s[0:1], 0, v[14:15]
	v_lshl_add_u64 v[2:3], v[2:3], 0, s[4:5]
	v_lshl_add_u64 v[4:5], v[4:5], 0, s[6:7]
	v_lshl_add_u64 v[6:7], v[6:7], 0, s[4:5]
	v_lshl_add_u64 v[8:9], v[8:9], 0, s[6:7]
	v_lshl_add_u64 v[10:11], v[10:11], 0, s[4:5]
	v_lshl_add_u64 v[12:13], v[12:13], 0, s[6:7]
	v_lshl_add_u64 v[14:15], v[14:15], 0, s[8:9]
	v_mov_b32_e32 v40, 0
	v_mov_b32_e32 v41, 0
	s_waitcnt vmcnt(9)
	v_max3_f32 v47, v44, v45, v46
	v_sub_f32_e32 v44, v44, v47
	v_sub_f32_e32 v45, v45, v47
	v_sub_f32_e32 v46, v46, v47
	v_mul_f32_e32 v44, 0x3fb8aa3b, v44
	v_mul_f32_e32 v45, 0x3fb8aa3b, v45
	v_mul_f32_e32 v46, 0x3fb8aa3b, v46
	v_exp_f32_e32 v44, v44
	v_exp_f32_e32 v45, v45
	v_exp_f32_e32 v47, v46
	s_waitcnt vmcnt(7)
	v_lshlrev_b32_e32 v32, 16, v20
	v_and_b32_e32 v33, 0xffff0000, v20
	v_add_f32_e32 v46, v44, v45
	v_add_f32_e32 v46, v47, v46
	v_div_scale_f32 v48, s[14:15], v46, v46, 1.0
	v_rcp_f32_e32 v50, v48
	v_div_scale_f32 v49, vcc, 1.0, v46, 1.0
	v_lshlrev_b32_e32 v20, 16, v21
	v_fma_f32 v51, -v48, v50, 1.0
	v_fmac_f32_e32 v50, v51, v50
	v_mul_f32_e32 v51, v49, v50
	v_fma_f32 v52, -v48, v51, v49
	v_fmac_f32_e32 v51, v52, v50
	v_fma_f32 v48, -v48, v51, v49
	v_div_fmas_f32 v48, v48, v50, v51
	v_div_fixup_f32 v48, v48, v46, 1.0
	v_and_b32_e32 v21, 0xffff0000, v21
	v_lshlrev_b32_e32 v34, 16, v22
	v_and_b32_e32 v35, 0xffff0000, v22
	v_lshlrev_b32_e32 v22, 16, v23
	v_and_b32_e32 v23, 0xffff0000, v23
	v_mul_f32_e32 v46, v45, v48
	v_lshlrev_b32_e32 v28, 16, v16
	v_and_b32_e32 v29, 0xffff0000, v16
	v_lshlrev_b32_e32 v16, 16, v17
	v_and_b32_e32 v17, 0xffff0000, v17
	v_lshlrev_b32_e32 v30, 16, v18
	v_and_b32_e32 v31, 0xffff0000, v18
	v_lshlrev_b32_e32 v18, 16, v19
	v_and_b32_e32 v19, 0xffff0000, v19
	v_mul_f32_e32 v44, v44, v48
	v_pk_mul_f32 v[32:33], v[46:47], v[32:33] op_sel_hi:[0,1]
	v_pk_mul_f32 v[20:21], v[46:47], v[20:21] op_sel_hi:[0,1]
	v_pk_mul_f32 v[34:35], v[46:47], v[34:35] op_sel_hi:[0,1]
	v_pk_mul_f32 v[22:23], v[46:47], v[22:23] op_sel_hi:[0,1]
	s_waitcnt vmcnt(6)
	v_lshlrev_b32_e32 v36, 16, v24
	v_and_b32_e32 v37, 0xffff0000, v24
	v_lshlrev_b32_e32 v38, 16, v26
	v_and_b32_e32 v39, 0xffff0000, v26
	v_mul_f32_e32 v48, v47, v48
	v_pk_fma_f32 v[16:17], v[44:45], v[16:17], v[20:21] op_sel_hi:[0,1,1]
	v_pk_fma_f32 v[20:21], v[44:45], v[28:29], v[32:33] op_sel_hi:[0,1,1]
	v_pk_fma_f32 v[18:19], v[44:45], v[18:19], v[22:23] op_sel_hi:[0,1,1]
	v_pk_fma_f32 v[22:23], v[44:45], v[30:31], v[34:35] op_sel_hi:[0,1,1]
	v_pk_fma_f32 v[20:21], v[48:49], v[36:37], v[20:21] op_sel_hi:[0,1,1]
	v_pk_fma_f32 v[22:23], v[48:49], v[38:39], v[22:23] op_sel_hi:[0,1,1]
	v_pk_mul_f32 v[20:21], v[20:21], s[10:11] op_sel_hi:[1,0]
	v_pk_mul_f32 v[22:23], v[22:23], s[10:11] op_sel_hi:[1,0]
	v_med3_f32 v20, v20, s11, v1
	v_med3_f32 v22, v22, s11, v1
	v_med3_f32 v21, v21, s11, v1
	v_med3_f32 v23, v23, s11, v1
	v_lshlrev_b32_e32 v24, 16, v25
	v_and_b32_e32 v25, 0xffff0000, v25
	v_lshlrev_b32_e32 v26, 16, v27
	v_and_b32_e32 v27, 0xffff0000, v27
	v_cvt_pk_fp8_f32 v40, v20, v21
	v_cvt_pk_fp8_f32 v41, v22, v23
	v_pk_fma_f32 v[16:17], v[48:49], v[24:25], v[16:17] op_sel_hi:[0,1,1]
	v_pk_fma_f32 v[18:19], v[48:49], v[26:27], v[18:19] op_sel_hi:[0,1,1]
	v_pk_mul_f32 v[16:17], v[16:17], s[10:11] op_sel_hi:[1,0]
	v_pk_mul_f32 v[18:19], v[18:19], s[10:11] op_sel_hi:[1,0]
	v_med3_f32 v16, v16, s11, v1
	v_med3_f32 v18, v18, s11, v1
	v_med3_f32 v17, v17, s11, v1
	v_med3_f32 v19, v19, s11, v1
	v_cvt_pk_fp8_f32 v40, v16, v17 op_sel:[0,0,1]
	v_cvt_pk_fp8_f32 v41, v18, v19 op_sel:[0,0,1]
	global_store_dwordx2 v[42:43], v[40:41], off
	v_lshl_add_u64 v[28:29], s[0:1], 0, v[12:13]
	v_lshl_add_u64 v[30:31], s[0:1], 0, v[8:9]
	v_lshl_add_u64 v[32:33], s[0:1], 0, v[4:5]
	v_lshl_add_u64 v[34:35], s[0:1], 0, v[10:11]
	v_lshl_add_u64 v[36:37], s[0:1], 0, v[6:7]
	v_lshl_add_u64 v[38:39], s[0:1], 0, v[2:3]
	global_load_dword v44, v[28:29], off
	global_load_dword v45, v[30:31], off
	global_load_dword v46, v[32:33], off
	global_load_dwordx4 v[16:19], v[34:35], off
	global_load_dwordx4 v[20:23], v[36:37], off
	global_load_dwordx4 v[24:27], v[38:39], off
	s_add_i32 s12, s12, s56
	v_lshl_add_u64 v[42:43], s[0:1], 0, v[14:15]
	v_lshl_add_u64 v[2:3], v[2:3], 0, s[4:5]
	v_lshl_add_u64 v[4:5], v[4:5], 0, s[6:7]
	v_lshl_add_u64 v[6:7], v[6:7], 0, s[4:5]
	v_lshl_add_u64 v[8:9], v[8:9], 0, s[6:7]
	v_lshl_add_u64 v[10:11], v[10:11], 0, s[4:5]
	v_lshl_add_u64 v[12:13], v[12:13], 0, s[6:7]
	v_lshl_add_u64 v[14:15], v[14:15], 0, s[8:9]
	v_mov_b32_e32 v40, 0
	v_mov_b32_e32 v41, 0
	s_waitcnt vmcnt(10)
	v_max3_f32 v63, v60, v61, v62
	v_sub_f32_e32 v60, v60, v63
	v_sub_f32_e32 v61, v61, v63
	v_sub_f32_e32 v62, v62, v63
	v_mul_f32_e32 v60, 0x3fb8aa3b, v60
	v_mul_f32_e32 v61, 0x3fb8aa3b, v61
	v_mul_f32_e32 v62, 0x3fb8aa3b, v62
	v_exp_f32_e32 v60, v60
	v_exp_f32_e32 v61, v61
	v_exp_f32_e32 v63, v62
	s_waitcnt vmcnt(8)
	v_lshlrev_b32_e32 v32, 16, v68
	v_and_b32_e32 v33, 0xffff0000, v68
	v_add_f32_e32 v62, v60, v61
	v_add_f32_e32 v62, v63, v62
	v_div_scale_f32 v48, s[14:15], v62, v62, 1.0
	v_rcp_f32_e32 v50, v48
	v_div_scale_f32 v49, vcc, 1.0, v62, 1.0
	v_lshlrev_b32_e32 v68, 16, v69
	v_fma_f32 v51, -v48, v50, 1.0
	v_fmac_f32_e32 v50, v51, v50
	v_mul_f32_e32 v51, v49, v50
	v_fma_f32 v52, -v48, v51, v49
	v_fmac_f32_e32 v51, v52, v50
	v_fma_f32 v48, -v48, v51, v49
	v_div_fmas_f32 v48, v48, v50, v51
	v_div_fixup_f32 v48, v48, v62, 1.0
	v_and_b32_e32 v69, 0xffff0000, v69
	v_lshlrev_b32_e32 v34, 16, v70
	v_and_b32_e32 v35, 0xffff0000, v70
	v_lshlrev_b32_e32 v70, 16, v71
	v_and_b32_e32 v71, 0xffff0000, v71
	v_mul_f32_e32 v62, v61, v48
	v_lshlrev_b32_e32 v28, 16, v64
	v_and_b32_e32 v29, 0xffff0000, v64
	v_lshlrev_b32_e32 v64, 16, v65
	v_and_b32_e32 v65, 0xffff0000, v65
	v_lshlrev_b32_e32 v30, 16, v66
	v_and_b32_e32 v31, 0xffff0000, v66
	v_lshlrev_b32_e32 v66, 16, v67
	v_and_b32_e32 v67, 0xffff0000, v67
	v_mul_f32_e32 v60, v60, v48
	v_pk_mul_f32 v[32:33], v[62:63], v[32:33] op_sel_hi:[0,1]
	v_pk_mul_f32 v[68:69], v[62:63], v[68:69] op_sel_hi:[0,1]
	v_pk_mul_f32 v[34:35], v[62:63], v[34:35] op_sel_hi:[0,1]
	v_pk_mul_f32 v[70:71], v[62:63], v[70:71] op_sel_hi:[0,1]
	s_waitcnt vmcnt(7)
	v_lshlrev_b32_e32 v36, 16, v72
	v_and_b32_e32 v37, 0xffff0000, v72
	v_lshlrev_b32_e32 v38, 16, v74
	v_and_b32_e32 v39, 0xffff0000, v74
	v_mul_f32_e32 v48, v63, v48
	v_pk_fma_f32 v[64:65], v[60:61], v[64:65], v[68:69] op_sel_hi:[0,1,1]
	v_pk_fma_f32 v[68:69], v[60:61], v[28:29], v[32:33] op_sel_hi:[0,1,1]
	v_pk_fma_f32 v[66:67], v[60:61], v[66:67], v[70:71] op_sel_hi:[0,1,1]
	v_pk_fma_f32 v[70:71], v[60:61], v[30:31], v[34:35] op_sel_hi:[0,1,1]
	v_pk_fma_f32 v[68:69], v[48:49], v[36:37], v[68:69] op_sel_hi:[0,1,1]
	v_pk_fma_f32 v[70:71], v[48:49], v[38:39], v[70:71] op_sel_hi:[0,1,1]
	v_pk_mul_f32 v[68:69], v[68:69], s[10:11] op_sel_hi:[1,0]
	v_pk_mul_f32 v[70:71], v[70:71], s[10:11] op_sel_hi:[1,0]
	v_med3_f32 v68, v68, s11, v1
	v_med3_f32 v70, v70, s11, v1
	v_med3_f32 v69, v69, s11, v1
	v_med3_f32 v71, v71, s11, v1
	v_lshlrev_b32_e32 v72, 16, v73
	v_and_b32_e32 v73, 0xffff0000, v73
	v_lshlrev_b32_e32 v74, 16, v75
	v_and_b32_e32 v75, 0xffff0000, v75
	v_cvt_pk_fp8_f32 v40, v68, v69
	v_cvt_pk_fp8_f32 v41, v70, v71
	v_pk_fma_f32 v[64:65], v[48:49], v[72:73], v[64:65] op_sel_hi:[0,1,1]
	v_pk_fma_f32 v[66:67], v[48:49], v[74:75], v[66:67] op_sel_hi:[0,1,1]
	v_pk_mul_f32 v[64:65], v[64:65], s[10:11] op_sel_hi:[1,0]
	v_pk_mul_f32 v[66:67], v[66:67], s[10:11] op_sel_hi:[1,0]
	v_med3_f32 v64, v64, s11, v1
	v_med3_f32 v66, v66, s11, v1
	v_med3_f32 v65, v65, s11, v1
	v_med3_f32 v67, v67, s11, v1
	v_cvt_pk_fp8_f32 v40, v64, v65 op_sel:[0,0,1]
	v_cvt_pk_fp8_f32 v41, v66, v67 op_sel:[0,0,1]
	global_store_dwordx2 v[58:59], v[40:41], off
	v_lshl_add_u64 v[28:29], s[0:1], 0, v[12:13]
	v_lshl_add_u64 v[30:31], s[0:1], 0, v[8:9]
	v_lshl_add_u64 v[32:33], s[0:1], 0, v[4:5]
	v_lshl_add_u64 v[34:35], s[0:1], 0, v[10:11]
	v_lshl_add_u64 v[36:37], s[0:1], 0, v[6:7]
	v_lshl_add_u64 v[38:39], s[0:1], 0, v[2:3]
	global_load_dword v60, v[28:29], off
	global_load_dword v61, v[30:31], off
	global_load_dword v62, v[32:33], off
	global_load_dwordx4 v[64:67], v[34:35], off
	global_load_dwordx4 v[68:71], v[36:37], off
	global_load_dwordx4 v[72:75], v[38:39], off
	s_add_i32 s12, s12, s56
	v_lshl_add_u64 v[58:59], s[0:1], 0, v[14:15]
	v_lshl_add_u64 v[2:3], v[2:3], 0, s[4:5]
	v_lshl_add_u64 v[4:5], v[4:5], 0, s[6:7]
	v_lshl_add_u64 v[6:7], v[6:7], 0, s[4:5]
	v_lshl_add_u64 v[8:9], v[8:9], 0, s[6:7]
	v_lshl_add_u64 v[10:11], v[10:11], 0, s[4:5]
	v_lshl_add_u64 v[12:13], v[12:13], 0, s[6:7]
	v_lshl_add_u64 v[14:15], v[14:15], 0, s[8:9]
	v_mov_b32_e32 v40, 0
	v_mov_b32_e32 v41, 0
	s_waitcnt vmcnt(10)
	v_max3_f32 v47, v44, v45, v46
	v_sub_f32_e32 v44, v44, v47
	v_sub_f32_e32 v45, v45, v47
	v_sub_f32_e32 v46, v46, v47
	v_mul_f32_e32 v44, 0x3fb8aa3b, v44
	v_mul_f32_e32 v45, 0x3fb8aa3b, v45
	v_mul_f32_e32 v46, 0x3fb8aa3b, v46
	v_exp_f32_e32 v44, v44
	v_exp_f32_e32 v45, v45
	v_exp_f32_e32 v47, v46
	s_waitcnt vmcnt(8)
	v_lshlrev_b32_e32 v32, 16, v20
	v_and_b32_e32 v33, 0xffff0000, v20
	v_add_f32_e32 v46, v44, v45
	v_add_f32_e32 v46, v47, v46
	v_div_scale_f32 v48, s[14:15], v46, v46, 1.0
	v_rcp_f32_e32 v50, v48
	v_div_scale_f32 v49, vcc, 1.0, v46, 1.0
	v_lshlrev_b32_e32 v20, 16, v21
	v_fma_f32 v51, -v48, v50, 1.0
	v_fmac_f32_e32 v50, v51, v50
	v_mul_f32_e32 v51, v49, v50
	v_fma_f32 v52, -v48, v51, v49
	v_fmac_f32_e32 v51, v52, v50
	v_fma_f32 v48, -v48, v51, v49
	v_div_fmas_f32 v48, v48, v50, v51
	v_div_fixup_f32 v48, v48, v46, 1.0
	v_and_b32_e32 v21, 0xffff0000, v21
	v_lshlrev_b32_e32 v34, 16, v22
	v_and_b32_e32 v35, 0xffff0000, v22
	v_lshlrev_b32_e32 v22, 16, v23
	v_and_b32_e32 v23, 0xffff0000, v23
	v_mul_f32_e32 v46, v45, v48
	v_lshlrev_b32_e32 v28, 16, v16
	v_and_b32_e32 v29, 0xffff0000, v16
	v_lshlrev_b32_e32 v16, 16, v17
	v_and_b32_e32 v17, 0xffff0000, v17
	v_lshlrev_b32_e32 v30, 16, v18
	v_and_b32_e32 v31, 0xffff0000, v18
	v_lshlrev_b32_e32 v18, 16, v19
	v_and_b32_e32 v19, 0xffff0000, v19
	v_mul_f32_e32 v44, v44, v48
	v_pk_mul_f32 v[32:33], v[46:47], v[32:33] op_sel_hi:[0,1]
	v_pk_mul_f32 v[20:21], v[46:47], v[20:21] op_sel_hi:[0,1]
	v_pk_mul_f32 v[34:35], v[46:47], v[34:35] op_sel_hi:[0,1]
	v_pk_mul_f32 v[22:23], v[46:47], v[22:23] op_sel_hi:[0,1]
	s_waitcnt vmcnt(7)
	v_lshlrev_b32_e32 v36, 16, v24
	v_and_b32_e32 v37, 0xffff0000, v24
	v_lshlrev_b32_e32 v38, 16, v26
	v_and_b32_e32 v39, 0xffff0000, v26
	v_mul_f32_e32 v48, v47, v48
	v_pk_fma_f32 v[16:17], v[44:45], v[16:17], v[20:21] op_sel_hi:[0,1,1]
	v_pk_fma_f32 v[20:21], v[44:45], v[28:29], v[32:33] op_sel_hi:[0,1,1]
	v_pk_fma_f32 v[18:19], v[44:45], v[18:19], v[22:23] op_sel_hi:[0,1,1]
	v_pk_fma_f32 v[22:23], v[44:45], v[30:31], v[34:35] op_sel_hi:[0,1,1]
	v_pk_fma_f32 v[20:21], v[48:49], v[36:37], v[20:21] op_sel_hi:[0,1,1]
	v_pk_fma_f32 v[22:23], v[48:49], v[38:39], v[22:23] op_sel_hi:[0,1,1]
	v_pk_mul_f32 v[20:21], v[20:21], s[10:11] op_sel_hi:[1,0]
	v_pk_mul_f32 v[22:23], v[22:23], s[10:11] op_sel_hi:[1,0]
	v_med3_f32 v20, v20, s11, v1
	v_med3_f32 v22, v22, s11, v1
	v_med3_f32 v21, v21, s11, v1
	v_med3_f32 v23, v23, s11, v1
	v_lshlrev_b32_e32 v24, 16, v25
	v_and_b32_e32 v25, 0xffff0000, v25
	v_lshlrev_b32_e32 v26, 16, v27
	v_and_b32_e32 v27, 0xffff0000, v27
	v_cvt_pk_fp8_f32 v40, v20, v21
	v_cvt_pk_fp8_f32 v41, v22, v23
	v_pk_fma_f32 v[16:17], v[48:49], v[24:25], v[16:17] op_sel_hi:[0,1,1]
	v_pk_fma_f32 v[18:19], v[48:49], v[26:27], v[18:19] op_sel_hi:[0,1,1]
	v_pk_mul_f32 v[16:17], v[16:17], s[10:11] op_sel_hi:[1,0]
	v_pk_mul_f32 v[18:19], v[18:19], s[10:11] op_sel_hi:[1,0]
	v_med3_f32 v16, v16, s11, v1
	v_med3_f32 v18, v18, s11, v1
	v_med3_f32 v17, v17, s11, v1
	v_med3_f32 v19, v19, s11, v1
	v_cvt_pk_fp8_f32 v40, v16, v17 op_sel:[0,0,1]
	v_cvt_pk_fp8_f32 v41, v18, v19 op_sel:[0,0,1]
	global_store_dwordx2 v[42:43], v[40:41], off
	v_mov_b32_e32 v40, 0
	v_mov_b32_e32 v41, 0
	s_waitcnt vmcnt(4)
	v_max3_f32 v63, v60, v61, v62
	v_sub_f32_e32 v60, v60, v63
	v_sub_f32_e32 v61, v61, v63
	v_sub_f32_e32 v62, v62, v63
	v_mul_f32_e32 v60, 0x3fb8aa3b, v60
	v_mul_f32_e32 v61, 0x3fb8aa3b, v61
	v_mul_f32_e32 v62, 0x3fb8aa3b, v62
	v_exp_f32_e32 v60, v60
	v_exp_f32_e32 v61, v61
	v_exp_f32_e32 v63, v62
	s_waitcnt vmcnt(2)
	v_lshlrev_b32_e32 v32, 16, v68
	v_and_b32_e32 v33, 0xffff0000, v68
	v_add_f32_e32 v62, v60, v61
	v_add_f32_e32 v62, v63, v62
	v_div_scale_f32 v48, s[14:15], v62, v62, 1.0
	v_rcp_f32_e32 v50, v48
	v_div_scale_f32 v49, vcc, 1.0, v62, 1.0
	v_lshlrev_b32_e32 v68, 16, v69
	v_fma_f32 v51, -v48, v50, 1.0
	v_fmac_f32_e32 v50, v51, v50
	v_mul_f32_e32 v51, v49, v50
	v_fma_f32 v52, -v48, v51, v49
	v_fmac_f32_e32 v51, v52, v50
	v_fma_f32 v48, -v48, v51, v49
	v_div_fmas_f32 v48, v48, v50, v51
	v_div_fixup_f32 v48, v48, v62, 1.0
	v_and_b32_e32 v69, 0xffff0000, v69
	v_lshlrev_b32_e32 v34, 16, v70
	v_and_b32_e32 v35, 0xffff0000, v70
	v_lshlrev_b32_e32 v70, 16, v71
	v_and_b32_e32 v71, 0xffff0000, v71
	v_mul_f32_e32 v62, v61, v48
	v_lshlrev_b32_e32 v28, 16, v64
	v_and_b32_e32 v29, 0xffff0000, v64
	v_lshlrev_b32_e32 v64, 16, v65
	v_and_b32_e32 v65, 0xffff0000, v65
	v_lshlrev_b32_e32 v30, 16, v66
	v_and_b32_e32 v31, 0xffff0000, v66
	v_lshlrev_b32_e32 v66, 16, v67
	v_and_b32_e32 v67, 0xffff0000, v67
	v_mul_f32_e32 v60, v60, v48
	v_pk_mul_f32 v[32:33], v[62:63], v[32:33] op_sel_hi:[0,1]
	v_pk_mul_f32 v[68:69], v[62:63], v[68:69] op_sel_hi:[0,1]
	v_pk_mul_f32 v[34:35], v[62:63], v[34:35] op_sel_hi:[0,1]
	v_pk_mul_f32 v[70:71], v[62:63], v[70:71] op_sel_hi:[0,1]
	s_waitcnt vmcnt(1)
	v_lshlrev_b32_e32 v36, 16, v72
	v_and_b32_e32 v37, 0xffff0000, v72
	v_lshlrev_b32_e32 v38, 16, v74
	v_and_b32_e32 v39, 0xffff0000, v74
	v_mul_f32_e32 v48, v63, v48
	v_pk_fma_f32 v[64:65], v[60:61], v[64:65], v[68:69] op_sel_hi:[0,1,1]
	v_pk_fma_f32 v[68:69], v[60:61], v[28:29], v[32:33] op_sel_hi:[0,1,1]
	v_pk_fma_f32 v[66:67], v[60:61], v[66:67], v[70:71] op_sel_hi:[0,1,1]
	v_pk_fma_f32 v[70:71], v[60:61], v[30:31], v[34:35] op_sel_hi:[0,1,1]
	v_pk_fma_f32 v[68:69], v[48:49], v[36:37], v[68:69] op_sel_hi:[0,1,1]
	v_pk_fma_f32 v[70:71], v[48:49], v[38:39], v[70:71] op_sel_hi:[0,1,1]
	v_pk_mul_f32 v[68:69], v[68:69], s[10:11] op_sel_hi:[1,0]
	v_pk_mul_f32 v[70:71], v[70:71], s[10:11] op_sel_hi:[1,0]
	v_med3_f32 v68, v68, s11, v1
	v_med3_f32 v70, v70, s11, v1
	v_med3_f32 v69, v69, s11, v1
	v_med3_f32 v71, v71, s11, v1
	v_lshlrev_b32_e32 v72, 16, v73
	v_and_b32_e32 v73, 0xffff0000, v73
	v_lshlrev_b32_e32 v74, 16, v75
	v_and_b32_e32 v75, 0xffff0000, v75
	v_cvt_pk_fp8_f32 v40, v68, v69
	v_cvt_pk_fp8_f32 v41, v70, v71
	v_pk_fma_f32 v[64:65], v[48:49], v[72:73], v[64:65] op_sel_hi:[0,1,1]
	v_pk_fma_f32 v[66:67], v[48:49], v[74:75], v[66:67] op_sel_hi:[0,1,1]
	v_pk_mul_f32 v[64:65], v[64:65], s[10:11] op_sel_hi:[1,0]
	v_pk_mul_f32 v[66:67], v[66:67], s[10:11] op_sel_hi:[1,0]
	v_med3_f32 v64, v64, s11, v1
	v_med3_f32 v66, v66, s11, v1
	v_med3_f32 v65, v65, s11, v1
	v_med3_f32 v67, v67, s11, v1
	v_cvt_pk_fp8_f32 v40, v64, v65 op_sel:[0,0,1]
	v_cvt_pk_fp8_f32 v41, v66, v67 op_sel:[0,0,1]
	global_store_dwordx2 v[58:59], v[40:41], off
